# hoisted four-waves-per-row scanner whose hit path skips the per-lane capacity check while the raw list is known to fit (scalar test), checked path out of line
# baseline (speedup 1.0000x reference)
.Lsc_go:
	s_add_i32 s41, s35, 1
	s_and_b32 s41, s41, 3
	s_lshl_b32 s40, s41, 2
	s_add_u32 s40, s40, s46
	v_mov_b32_e32 v27, s40
	ds_read_b32 v26, v27
	s_mov_b32 s42, 0
	s_waitcnt vmcnt(9)
	v_or3_b32 v12, v100, v101, v102
	v_bitop3_b32 v12, v12, s9, v103 bitop3:0xc8
	v_cmp_ne_u32_e32 vcc, 0, v12
	s_and_b64 vcc, vcc, s[48:49]
	s_cbranch_vccz .Lsc_s0
	s_bcnt1_i32_b64 s40, vcc
	v_mbcnt_lo_u32_b32 v13, vcc_lo, 0
	v_mbcnt_hi_u32_b32 v13, vcc_hi, v13
	v_add_u32_e32 v13, s42, v13
	s_add_i32 s42, s42, s40
	s_cmp_gt_u32 s42, 64
	s_cbranch_scc1 .Lsc_c0
	s_mov_b64 exec, vcc
.Lsc_w0:
	v_lshl_add_u32 v14, v13, 4, v9
	v_lshl_add_u32 v15, v13, 2, v10
	v_mov_b32_e32 v13, v8
	ds_write_b128 v14, v[100:103]
	ds_write_b32 v15, v13
	s_mov_b64 exec, -1
.Lsc_s0:
	s_mov_b32 s40, s39
	buffer_load_dwordx4 v[100:103], v5, s[28:31], s40 offen nt
	s_waitcnt vmcnt(9)
	v_or3_b32 v12, v104, v105, v106
	v_bitop3_b32 v12, v12, s9, v107 bitop3:0xc8
	v_cmp_ne_u32_e32 vcc, 0, v12
	s_cbranch_vccz .Lsc_s1
	s_bcnt1_i32_b64 s40, vcc
	v_mbcnt_lo_u32_b32 v13, vcc_lo, 0
	v_mbcnt_hi_u32_b32 v13, vcc_hi, v13
	v_add_u32_e32 v13, s42, v13
	s_add_i32 s42, s42, s40
	s_cmp_gt_u32 s42, 64
	s_cbranch_scc1 .Lsc_c1
	s_mov_b64 exec, vcc
.Lsc_w1:
	v_lshl_add_u32 v14, v13, 4, v9
	v_lshl_add_u32 v15, v13, 2, v10
	v_add_u32_e32 v13, 0x100, v8
	ds_write_b128 v14, v[104:107]
	ds_write_b32 v15, v13
	s_mov_b64 exec, -1
.Lsc_s1:
	s_add_u32 s40, s39, 0x400
	buffer_load_dwordx4 v[104:107], v6, s[28:31], s40 offen nt
	s_waitcnt vmcnt(9)
	v_or3_b32 v12, v108, v109, v110
	v_bitop3_b32 v12, v12, s9, v111 bitop3:0xc8
	v_cmp_ne_u32_e32 vcc, 0, v12
	s_cbranch_vccz .Lsc_s2
	s_bcnt1_i32_b64 s40, vcc
	v_mbcnt_lo_u32_b32 v13, vcc_lo, 0
	v_mbcnt_hi_u32_b32 v13, vcc_hi, v13
	v_add_u32_e32 v13, s42, v13
	s_add_i32 s42, s42, s40
	s_cmp_gt_u32 s42, 64
	s_cbranch_scc1 .Lsc_c2
	s_mov_b64 exec, vcc
.Lsc_w2:
	v_lshl_add_u32 v14, v13, 4, v9
	v_lshl_add_u32 v15, v13, 2, v10
	v_add_u32_e32 v13, 0x200, v8
	ds_write_b128 v14, v[108:111]
	ds_write_b32 v15, v13
	s_mov_b64 exec, -1
.Lsc_s2:
	s_add_u32 s40, s39, 0x800
	buffer_load_dwordx4 v[108:111], v6, s[28:31], s40 offen nt
	s_waitcnt vmcnt(9)
	v_or3_b32 v12, v112, v113, v114
	v_bitop3_b32 v12, v12, s9, v115 bitop3:0xc8
	v_cmp_ne_u32_e32 vcc, 0, v12
	s_cbranch_vccz .Lsc_s3
	s_bcnt1_i32_b64 s40, vcc
	v_mbcnt_lo_u32_b32 v13, vcc_lo, 0
	v_mbcnt_hi_u32_b32 v13, vcc_hi, v13
	v_add_u32_e32 v13, s42, v13
	s_add_i32 s42, s42, s40
	s_cmp_gt_u32 s42, 64
	s_cbranch_scc1 .Lsc_c3
	s_mov_b64 exec, vcc
.Lsc_w3:
	v_lshl_add_u32 v14, v13, 4, v9
	v_lshl_add_u32 v15, v13, 2, v10
	v_add_u32_e32 v13, 0x300, v8
	ds_write_b128 v14, v[112:115]
	ds_write_b32 v15, v13
	s_mov_b64 exec, -1
.Lsc_s3:
	s_add_u32 s40, s39, 0xc00
	buffer_load_dwordx4 v[112:115], v6, s[28:31], s40 offen nt
	s_waitcnt vmcnt(9)
	v_or3_b32 v12, v116, v117, v118
	v_bitop3_b32 v12, v12, s9, v119 bitop3:0xc8
	v_cmp_ne_u32_e32 vcc, 0, v12
	s_cbranch_vccz .Lsc_s4
	s_bcnt1_i32_b64 s40, vcc
	v_mbcnt_lo_u32_b32 v13, vcc_lo, 0
	v_mbcnt_hi_u32_b32 v13, vcc_hi, v13
	v_add_u32_e32 v13, s42, v13
	s_add_i32 s42, s42, s40
	s_cmp_gt_u32 s42, 64
	s_cbranch_scc1 .Lsc_c4
	s_mov_b64 exec, vcc
.Lsc_w4:
	v_lshl_add_u32 v14, v13, 4, v9
	v_lshl_add_u32 v15, v13, 2, v10
	v_add_u32_e32 v13, 0x400, v8
	ds_write_b128 v14, v[116:119]
	ds_write_b32 v15, v13
	s_mov_b64 exec, -1
.Lsc_s4:
	s_add_u32 s40, s39, 0x1000
	buffer_load_dwordx4 v[116:119], v6, s[28:31], s40 offen nt
	s_waitcnt vmcnt(9)
	v_or3_b32 v12, v120, v121, v122
	v_bitop3_b32 v12, v12, s9, v123 bitop3:0xc8
	v_cmp_ne_u32_e32 vcc, 0, v12
	s_cbranch_vccz .Lsc_s5
	s_bcnt1_i32_b64 s40, vcc
	v_mbcnt_lo_u32_b32 v13, vcc_lo, 0
	v_mbcnt_hi_u32_b32 v13, vcc_hi, v13
	v_add_u32_e32 v13, s42, v13
	s_add_i32 s42, s42, s40
	s_cmp_gt_u32 s42, 64
	s_cbranch_scc1 .Lsc_c5
	s_mov_b64 exec, vcc
.Lsc_w5:
	v_lshl_add_u32 v14, v13, 4, v9
	v_lshl_add_u32 v15, v13, 2, v10
	v_add_u32_e32 v13, 0x500, v8
	ds_write_b128 v14, v[120:123]
	ds_write_b32 v15, v13
	s_mov_b64 exec, -1
.Lsc_s5:
	s_add_u32 s40, s39, 0x1400
	buffer_load_dwordx4 v[120:123], v6, s[28:31], s40 offen nt
	s_waitcnt vmcnt(9)
	v_or3_b32 v12, v124, v125, v126
	v_bitop3_b32 v12, v12, s9, v127 bitop3:0xc8
	v_cmp_ne_u32_e32 vcc, 0, v12
	s_cbranch_vccz .Lsc_s6
	s_bcnt1_i32_b64 s40, vcc
	v_mbcnt_lo_u32_b32 v13, vcc_lo, 0
	v_mbcnt_hi_u32_b32 v13, vcc_hi, v13
	v_add_u32_e32 v13, s42, v13
	s_add_i32 s42, s42, s40
	s_cmp_gt_u32 s42, 64
	s_cbranch_scc1 .Lsc_c6
	s_mov_b64 exec, vcc
.Lsc_w6:
	v_lshl_add_u32 v14, v13, 4, v9
	v_lshl_add_u32 v15, v13, 2, v10
	v_add_u32_e32 v13, 0x600, v8
	ds_write_b128 v14, v[124:127]
	ds_write_b32 v15, v13
	s_mov_b64 exec, -1
.Lsc_s6:
	s_add_u32 s40, s39, 0x1800
	buffer_load_dwordx4 v[124:127], v6, s[28:31], s40 offen nt
	s_waitcnt vmcnt(9)
	v_or3_b32 v12, v128, v129, v130
	v_bitop3_b32 v12, v12, s9, v131 bitop3:0xc8
	v_cmp_ne_u32_e32 vcc, 0, v12
	s_cbranch_vccz .Lsc_s7
	s_bcnt1_i32_b64 s40, vcc
	v_mbcnt_lo_u32_b32 v13, vcc_lo, 0
	v_mbcnt_hi_u32_b32 v13, vcc_hi, v13
	v_add_u32_e32 v13, s42, v13
	s_add_i32 s42, s42, s40
	s_cmp_gt_u32 s42, 64
	s_cbranch_scc1 .Lsc_c7
	s_mov_b64 exec, vcc
.Lsc_w7:
	v_lshl_add_u32 v14, v13, 4, v9
	v_lshl_add_u32 v15, v13, 2, v10
	v_add_u32_e32 v13, 0x700, v8
	ds_write_b128 v14, v[128:131]
	ds_write_b32 v15, v13
	s_mov_b64 exec, -1
.Lsc_s7:
	s_add_u32 s40, s39, 0x1c00
	buffer_load_dwordx4 v[128:131], v6, s[28:31], s40 offen nt
	s_waitcnt vmcnt(9)
	v_or3_b32 v12, v132, v133, v134
	v_bitop3_b32 v12, v12, s9, v135 bitop3:0xc8
	v_cmp_ne_u32_e32 vcc, 0, v12
	s_cbranch_vccz .Lsc_s8
	s_bcnt1_i32_b64 s40, vcc
	v_mbcnt_lo_u32_b32 v13, vcc_lo, 0
	v_mbcnt_hi_u32_b32 v13, vcc_hi, v13
	v_add_u32_e32 v13, s42, v13
	s_add_i32 s42, s42, s40
	s_cmp_gt_u32 s42, 64
	s_cbranch_scc1 .Lsc_c8
	s_mov_b64 exec, vcc
.Lsc_w8:
	v_lshl_add_u32 v14, v13, 4, v9
	v_lshl_add_u32 v15, v13, 2, v10
	v_add_u32_e32 v13, 0x800, v8
	ds_write_b128 v14, v[132:135]
	ds_write_b32 v15, v13
	s_mov_b64 exec, -1
.Lsc_s8:
	s_add_u32 s40, s39, 0x2000
	buffer_load_dwordx4 v[132:135], v6, s[28:31], s40 offen nt
	s_waitcnt vmcnt(9)
	v_or3_b32 v12, v136, v137, v138
	v_bitop3_b32 v12, v12, s9, v139 bitop3:0xc8
	v_cmp_ne_u32_e32 vcc, 0, v12
	s_and_b64 vcc, vcc, s[50:51]
	s_cbranch_vccz .Lsc_s9
	s_bcnt1_i32_b64 s40, vcc
	v_mbcnt_lo_u32_b32 v13, vcc_lo, 0
	v_mbcnt_hi_u32_b32 v13, vcc_hi, v13
	v_add_u32_e32 v13, s42, v13
	s_add_i32 s42, s42, s40
	s_cmp_gt_u32 s42, 64
	s_cbranch_scc1 .Lsc_c9
	s_mov_b64 exec, vcc
.Lsc_w9:
	v_lshl_add_u32 v14, v13, 4, v9
	v_lshl_add_u32 v15, v13, 2, v10
	v_add_u32_e32 v13, 0x900, v8
	ds_write_b128 v14, v[136:139]
	ds_write_b32 v15, v13
	s_mov_b64 exec, -1

.Lsc_c0:
	v_cmp_gt_i32_e64 s[0:1], s7, v13
	s_and_b64 s[4:5], vcc, s[0:1]
	s_mov_b64 exec, s[4:5]
	s_branch .Lsc_w0
